# P10/P11: build_tab skipped when phase 9 already left the expert tables in LDS (ph_lo <= 9)
# baseline (speedup 1.0000x reference)
; #define LAS __attribute__((address_space(3)))
; __device__ __forceinline__ void build_tab(Frame& F) {
;     LAS int* tab = (LAS int*)(F.lds + TAB_OFF); LAS int* rp = (LAS int*)(F.lds + RP_OFF);
;     if (F.tid < NE) { const unsigned* cnt = WSP(unsigned, WS_CTL) + CW_CNT; int run = 0;
; #pragma unroll
;         for (int r = 0; r < RR; ++r) { rp[F.tid * RR + r] = run; run += (int)__hip_atomic_load(cnt + (r * NE + F.tid) * 16, __ATOMIC_RELAXED, __HIP_MEMORY_SCOPE_AGENT); }
;         tab[64 + F.tid] = run; }
.LBB0_1069:
	s_cmp_lt_i32 s66, 11
	s_cselect_b64 s[0:1], -1, 0
	s_cmp_gt_i32 s67, 10
	s_cselect_b64 s[2:3], -1, 0
	s_and_b64 s[0:1], s[0:1], s[2:3]
	s_andn2_b64 vcc, exec, s[0:1]
	s_cbranch_vccnz .LBB0_1208
	s_cmp_lt_i32 s66, 10
	s_cbranch_scc1 .Lp10_tab_ok
	v_cmp_gt_u32_e32 vcc, 32, v0
	s_and_saveexec_b64 s[0:1], vcc
	s_cbranch_execz .LBB0_1072
	v_lshlrev_b32_e32 v2, 6, v0
	v_add_u32_e32 v3, 0, v2
	v_add_u32_e32 v6, 0x20300, v3
	v_mov_b32_e32 v3, 0
	ds_write_b32 v6, v3
	v_lshl_add_u64 v[2:3], s[96:97], 0, v[2:3]
	s_mov_b64 s[2:3], 0x8000
	v_lshl_add_u64 v[4:5], v[2:3], 0, s[2:3]
	s_mov_b64 s[2:3], 0x1000
	global_load_dword v8, v[4:5], off sc1
	global_load_dword v9, v[4:5], off offset:2048 sc1
	v_lshl_add_u64 v[4:5], v[4:5], 0, s[2:3]
	global_load_dword v10, v[4:5], off sc1
	global_load_dword v11, v[4:5], off offset:2048 sc1
	v_lshl_add_u64 v[4:5], v[4:5], 0, s[2:3]
	global_load_dword v242, v[4:5], off sc1
	global_load_dword v243, v[4:5], off offset:2048 sc1
	v_lshl_add_u64 v[4:5], v[4:5], 0, s[2:3]
	global_load_dword v244, v[4:5], off sc1
	global_load_dword v245, v[4:5], off offset:2048 sc1
	v_lshl_add_u64 v[4:5], v[4:5], 0, s[2:3]
	global_load_dword v246, v[4:5], off sc1
	global_load_dword v247, v[4:5], off offset:2048 sc1
	v_lshl_add_u64 v[4:5], v[4:5], 0, s[2:3]
	global_load_dword v248, v[4:5], off sc1
	global_load_dword v249, v[4:5], off offset:2048 sc1
	v_lshl_add_u64 v[4:5], v[4:5], 0, s[2:3]
	global_load_dword v250, v[4:5], off sc1
	global_load_dword v251, v[4:5], off offset:2048 sc1
	v_lshl_add_u64 v[4:5], v[4:5], 0, s[2:3]
	global_load_dword v252, v[4:5], off sc1
	global_load_dword v253, v[4:5], off offset:2048 sc1
	s_add_i32 s2, 0, 0x20100
	s_waitcnt vmcnt(0)
	ds_write_b32 v6, v8 offset:4
	v_add_u32_e32 v9, v9, v8
	ds_write_b32 v6, v9 offset:8
	v_add_u32_e32 v10, v10, v9
	ds_write_b32 v6, v10 offset:12
	v_add_u32_e32 v11, v11, v10
	ds_write_b32 v6, v11 offset:16
	v_add_u32_e32 v242, v242, v11
	ds_write_b32 v6, v242 offset:20
	v_add_u32_e32 v243, v243, v242
	ds_write_b32 v6, v243 offset:24
	v_add_u32_e32 v244, v244, v243
	ds_write_b32 v6, v244 offset:28
	v_add_u32_e32 v245, v245, v244
	ds_write_b32 v6, v245 offset:32
	v_add_u32_e32 v246, v246, v245
	ds_write_b32 v6, v246 offset:36
	v_add_u32_e32 v247, v247, v246
	ds_write_b32 v6, v247 offset:40
	v_add_u32_e32 v248, v248, v247
	ds_write_b32 v6, v248 offset:44
	v_add_u32_e32 v249, v249, v248
	ds_write_b32 v6, v249 offset:48
	v_add_u32_e32 v250, v250, v249
	ds_write_b32 v6, v250 offset:52
	v_add_u32_e32 v251, v251, v250
	ds_write_b32 v6, v251 offset:56
	v_add_u32_e32 v252, v252, v251
	ds_write_b32 v6, v252 offset:60
	v_add_u32_e32 v253, v253, v252
	v_lshl_add_u32 v3, v0, 2, s2
	ds_write_b32 v3, v253 offset:256

; #define LAS __attribute__((address_space(3)))
; __device__ __forceinline__ void build_tab(Frame& F) {
;     ...
;     __syncthreads();
; }
; __device__ __forceinline__ int build_list(Frame& F, int mode) {
;     LAS int* list = (LAS int*)(F.lds + LIST_OFF); const LAS int* tab = (const LAS int*)(F.lds + TAB_OFF);
;     int total;
;     if (mode == 0) total = 64 * 26 + 4 * 9; else if (mode == 1) total = 64 * 8; else total = (tab[32] / EB) * (mode == 2 ? 16 : 8);
;     const int c = F.bx; const int n = c < total ? (total - c + F.G - 1) / F.G : 0;
.Lp10_tab_ok:
	s_add_i32 s0, 0, 0x20180
	v_mov_b32_e32 v2, s0
	s_waitcnt lgkmcnt(0)
	s_barrier
	ds_read_b32 v2, v2
	s_mov_b32 s64, 0
	s_waitcnt lgkmcnt(0)
	v_readfirstlane_b32 s0, v2
	s_ashr_i32 s1, s0, 31
	s_lshr_b32 s1, s1, 24
	s_add_i32 s0, s0, s1
	s_ashr_i32 s2, s0, 8
	s_lshl_b32 s0, s2, 3
	s_cmp_ge_i32 s91, s0
	s_cbranch_scc1 .LBB0_1076
	s_abs_i32 s1, s79
	v_cvt_f32_u32_e32 v2, s1
	s_not_b32 s3, s91
	s_add_i32 s0, s0, s3
	s_sub_i32 s3, 0, s1
	v_rcp_iflag_f32_e32 v2, v2
	s_add_i32 s0, s0, s79
	s_xor_b32 s4, s0, s79
	s_abs_i32 s0, s0
	v_mul_f32_e32 v2, 0x4f7ffffe, v2
	v_cvt_u32_f32_e32 v2, v2
	s_ashr_i32 s4, s4, 31
	v_readfirstlane_b32 s5, v2
	s_mul_i32 s3, s3, s5
	s_mul_hi_u32 s3, s5, s3
	s_add_i32 s5, s5, s3
	s_mul_hi_u32 s3, s0, s5
	s_mul_i32 s5, s3, s1
	s_sub_i32 s0, s0, s5
	s_add_i32 s6, s3, 1
	s_sub_i32 s5, s0, s1
	s_cmp_ge_u32 s0, s1
	s_cselect_b32 s3, s6, s3
	s_cselect_b32 s0, s5, s0
	s_add_i32 s5, s3, 1
	s_cmp_ge_u32 s0, s1
	s_cselect_b32 s0, s5, s3
	s_xor_b32 s0, s0, s4
	s_sub_i32 s64, s0, s4

; #define LAS __attribute__((address_space(3)))
; __device__ __forceinline__ void build_tab(Frame& F) {
;     LAS int* tab = (LAS int*)(F.lds + TAB_OFF); LAS int* rp = (LAS int*)(F.lds + RP_OFF);
;     if (F.tid < NE) { const unsigned* cnt = WSP(unsigned, WS_CTL) + CW_CNT; int run = 0;
; #pragma unroll
;         for (int r = 0; r < RR; ++r) { rp[F.tid * RR + r] = run; run += (int)__hip_atomic_load(cnt + (r * NE + F.tid) * 16, __ATOMIC_RELAXED, __HIP_MEMORY_SCOPE_AGENT); }
;         tab[64 + F.tid] = run; }
.LBB0_1208:
	s_cmp_lt_i32 s66, 12
	s_cselect_b64 s[0:1], -1, 0
	s_cmp_gt_i32 s67, 11
	s_cselect_b64 s[2:3], -1, 0
	s_and_b64 s[0:1], s[0:1], s[2:3]
	s_andn2_b64 vcc, exec, s[0:1]
	s_cbranch_vccnz .LBB0_1216
	s_cmp_lt_i32 s66, 10
	s_cbranch_scc1 .Lp11_tab_ok
	v_cmp_gt_u32_e32 vcc, 32, v0
	s_and_saveexec_b64 s[0:1], vcc
	s_cbranch_execz .LBB0_1211
	v_lshlrev_b32_e32 v2, 6, v0
	v_add_u32_e32 v3, 0, v2
	v_add_u32_e32 v6, 0x20300, v3
	v_mov_b32_e32 v3, 0
	ds_write_b32 v6, v3
	v_lshl_add_u64 v[2:3], s[96:97], 0, v[2:3]
	s_mov_b64 s[2:3], 0x8000
	v_lshl_add_u64 v[4:5], v[2:3], 0, s[2:3]
	s_mov_b64 s[2:3], 0x1000
	global_load_dword v8, v[4:5], off sc1
	global_load_dword v9, v[4:5], off offset:2048 sc1
	v_lshl_add_u64 v[4:5], v[4:5], 0, s[2:3]
	global_load_dword v10, v[4:5], off sc1
	global_load_dword v11, v[4:5], off offset:2048 sc1
	v_lshl_add_u64 v[4:5], v[4:5], 0, s[2:3]
	global_load_dword v242, v[4:5], off sc1
	global_load_dword v243, v[4:5], off offset:2048 sc1
	v_lshl_add_u64 v[4:5], v[4:5], 0, s[2:3]
	global_load_dword v244, v[4:5], off sc1
	global_load_dword v245, v[4:5], off offset:2048 sc1
	v_lshl_add_u64 v[4:5], v[4:5], 0, s[2:3]
	global_load_dword v246, v[4:5], off sc1
	global_load_dword v247, v[4:5], off offset:2048 sc1
	v_lshl_add_u64 v[4:5], v[4:5], 0, s[2:3]
	global_load_dword v248, v[4:5], off sc1
	global_load_dword v249, v[4:5], off offset:2048 sc1
	v_lshl_add_u64 v[4:5], v[4:5], 0, s[2:3]
	global_load_dword v250, v[4:5], off sc1
	global_load_dword v251, v[4:5], off offset:2048 sc1
	v_lshl_add_u64 v[4:5], v[4:5], 0, s[2:3]
	global_load_dword v252, v[4:5], off sc1
	global_load_dword v253, v[4:5], off offset:2048 sc1
	s_add_i32 s2, 0, 0x20100
	v_lshl_add_u32 v0, v0, 2, s2
	s_waitcnt vmcnt(0)
	ds_write_b32 v6, v8 offset:4
	v_add_u32_e32 v9, v9, v8
	ds_write_b32 v6, v9 offset:8
	v_add_u32_e32 v10, v10, v9
	ds_write_b32 v6, v10 offset:12
	v_add_u32_e32 v11, v11, v10
	ds_write_b32 v6, v11 offset:16
	v_add_u32_e32 v242, v242, v11
	ds_write_b32 v6, v242 offset:20
	v_add_u32_e32 v243, v243, v242
	ds_write_b32 v6, v243 offset:24
	v_add_u32_e32 v244, v244, v243
	ds_write_b32 v6, v244 offset:28
	v_add_u32_e32 v245, v245, v244
	ds_write_b32 v6, v245 offset:32
	v_add_u32_e32 v246, v246, v245
	ds_write_b32 v6, v246 offset:36
	v_add_u32_e32 v247, v247, v246
	ds_write_b32 v6, v247 offset:40
	v_add_u32_e32 v248, v248, v247
	ds_write_b32 v6, v248 offset:44
	v_add_u32_e32 v249, v249, v248
	ds_write_b32 v6, v249 offset:48
	v_add_u32_e32 v250, v250, v249
	ds_write_b32 v6, v250 offset:52
	v_add_u32_e32 v251, v251, v250
	ds_write_b32 v6, v251 offset:56
	v_add_u32_e32 v252, v252, v251
	ds_write_b32 v6, v252 offset:60
	v_add_u32_e32 v253, v253, v252
	ds_write_b32 v0, v253 offset:256

; #define LAS __attribute__((address_space(3)))
; __device__ __forceinline__ void p11_final(Frame& F) {
;     build_tab(F);
;     const LAS int* tab = (const LAS int*)(F.lds + TAB_OFF); const LAS int* rp = (const LAS int*)(F.lds + RP_OFF);
;     const float* mod = WSP(float, WS_MOD); const bf16_t* X1 = WSP(bf16_t, WS_X1); const unsigned char* YM = WSP(unsigned char, WS_YM);
;     const int* tok_e = WSP(int, WS_ROUTE); const int* tok_rank = tok_e + M_LAT * TOPK; const float* tok_gate = (const float*)(tok_rank + M_LAT * TOPK);
;     const int gw = F.bx * NWAVES + F.wave, NGW = F.G * NWAVES;
;     for (int row = gw; row < M_LAT; row += NGW) {
;         const float* mr = mod + (row / T) * NMOD;
.Lp11_tab_ok:
	s_lshl_b32 s0, s91, 3
	v_readlane_b32 s1, v254, 35
	s_add_i32 s0, s0, s1
	s_cmpk_gt_i32 s0, 0x3fff
	s_waitcnt lgkmcnt(0)
	s_barrier
	s_cbranch_scc1 .LBB0_1216
	s_add_u32 s12, s96, 0x8ec00000
	s_addc_u32 s13, s97, 0
	s_add_u32 s14, s96, 0x8ec40000
	s_addc_u32 s15, s97, 0
	s_add_u32 s16, s96, 0x8ec80000
	s_addc_u32 s17, s97, 0
	s_lshl_b32 s4, s79, 3
	s_abs_i32 s1, s4
	v_cvt_f32_u32_e32 v0, s1
	s_sub_i32 s5, 0, s1
	s_add_i32 s2, s4, 0x3fff
	s_xor_b32 s3, s2, s4
	v_rcp_iflag_f32_e32 v0, v0
	s_abs_i32 s2, s2
	s_ashr_i32 s3, s3, 31
	v_lshlrev_b32_e32 v8, 2, v1
	v_mul_f32_e32 v0, 0x4f7ffffe, v0
	v_cvt_u32_f32_e32 v0, v0
	v_mov_b32_e32 v9, 0
	v_lshl_add_u64 v[2:3], s[96:97], 0, v[8:9]
	v_mov_b32_e32 v5, v9
	v_readfirstlane_b32 s6, v0
	s_mul_i32 s5, s5, s6
	s_mul_hi_u32 s5, s6, s5
	s_add_i32 s6, s6, s5
	s_mul_hi_u32 s5, s2, s6
	s_mul_i32 s6, s5, s1
	s_sub_i32 s2, s2, s6
	s_add_i32 s7, s5, 1
	s_sub_i32 s6, s2, s1
	s_cmp_ge_u32 s2, s1
	s_cselect_b32 s5, s7, s5
	s_cselect_b32 s2, s6, s2
	s_add_i32 s6, s5, 1
	s_cmp_ge_u32 s2, s1
	s_cselect_b32 s1, s6, s5
	s_xor_b32 s1, s1, s3
	s_sub_i32 s1, s1, s3
	s_lshl_b32 s1, s1, 3
	s_mov_b64 s[2:3], 0xb3400000
	v_lshl_add_u64 v[10:11], v[2:3], 0, s[2:3]
	s_add_u32 s2, s48, 0x6000
	v_or_b32_e32 v0, 0x100, v8
	s_addc_u32 s3, s49, 0
	v_lshlrev_b32_e32 v4, 2, v0
	s_abs_i32 s18, s1
	v_lshl_add_u64 v[14:15], s[2:3], 0, v[4:5]
	v_cvt_f32_u32_e32 v5, s18
	v_or_b32_e32 v4, 0x200, v8
	v_lshlrev_b32_e32 v6, 2, v4
	v_mov_b32_e32 v7, v9
	v_rcp_iflag_f32_e32 v5, v5
	v_lshl_add_u64 v[16:17], s[2:3], 0, v[6:7]
	v_or_b32_e32 v6, 0x300, v8
	v_or_b32_e32 v32, 0x400, v8
	v_mul_f32_e32 v5, 0x4f7ffffe, v5
	v_cvt_u32_f32_e32 v5, v5
	v_or_b32_e32 v34, 0x500, v8
	v_or_b32_e32 v36, 0x600, v8
	v_or_b32_e32 v38, 0x700, v8
	v_lshlrev_b32_e32 v2, 4, v1
	v_mov_b32_e32 v3, v9
	v_lshlrev_b32_e32 v18, 2, v6
	v_mov_b32_e32 v19, v9
	v_lshlrev_b32_e32 v20, 2, v32
	v_mov_b32_e32 v21, v9
	v_lshlrev_b32_e32 v22, 2, v34
	v_mov_b32_e32 v23, v9
	v_lshlrev_b32_e32 v24, 2, v36
	v_mov_b32_e32 v25, v9
	v_lshlrev_b32_e32 v26, 2, v38
	v_mov_b32_e32 v27, v9
	v_lshl_add_u64 v[12:13], s[2:3], 0, v[2:3]
	v_lshl_add_u64 v[18:19], s[2:3], 0, v[18:19]
	v_lshl_add_u64 v[20:21], s[2:3], 0, v[20:21]
	v_lshl_add_u64 v[22:23], s[2:3], 0, v[22:23]
	v_lshl_add_u64 v[24:25], s[2:3], 0, v[24:25]
	v_lshl_add_u64 v[26:27], s[2:3], 0, v[26:27]
	s_ashr_i32 s19, s1, 31
	s_sub_i32 s1, 0, s18
	v_readfirstlane_b32 s2, v5
	s_mul_i32 s1, s1, s2
	s_mul_hi_u32 s1, s2, s1
	s_add_i32 s20, s2, s1
	s_ashr_i32 s1, s0, 31
	s_lshl_b64 s[2:3], s[0:1], 12
	s_add_u32 s2, s96, s2
	v_lshlrev_b32_e32 v28, 3, v1
	v_mov_b32_e32 v29, v9
	s_addc_u32 s3, s97, s3
	v_lshl_add_u64 v[28:29], s[2:3], 0, v[28:29]
	s_mov_b64 s[2:3], 0x82c00000
	v_lshl_add_u64 v[28:29], v[28:29], 0, s[2:3]
	v_readlane_b32 s3, v254, 35
	s_lshl_b32 s2, s91, 5
	s_lshl_b32 s3, s3, 2
	v_readlane_b32 s24, v254, 0
	s_ashr_i32 s5, s4, 31
	s_add_i32 s2, s2, s3
	v_readlane_b32 s30, v254, 6
	v_readlane_b32 s31, v254, 7
	s_lshl_b64 s[6:7], s[4:5], 12
	s_or_b32 s2, s2, 3
	s_lshl_b32 s21, s79, 5
	s_lshl_b64 s[8:9], s[0:1], 13
	s_mov_b64 s[10:11], s[30:31]
	s_add_u32 s8, s10, s8
	s_addc_u32 s9, s11, s9
	v_lshl_add_u64 v[2:3], s[8:9], 0, v[2:3]
	s_mov_b64 s[8:9], 0x1000
	v_lshl_add_u64 v[30:31], v[2:3], 0, s[8:9]
	s_lshl_b64 s[8:9], s[4:5], 13
	s_add_i32 s1, 0, 0x20100
	v_mov_b32_e32 v56, 0x358637bd
	v_lshlrev_b32_e32 v57, 2, v8
	v_lshlrev_b32_e32 v58, 2, v0
	v_lshlrev_b32_e32 v59, 2, v4
	v_lshlrev_b32_e32 v60, 2, v6
	v_lshlrev_b32_e32 v61, 2, v32
	v_lshlrev_b32_e32 v62, 2, v34
	v_lshlrev_b32_e32 v63, 2, v36
	v_lshlrev_b32_e32 v64, 2, v38
	v_readlane_b32 s25, v254, 1
	v_readlane_b32 s26, v254, 2
	v_readlane_b32 s27, v254, 3
	v_readlane_b32 s28, v254, 4
	v_readlane_b32 s29, v254, 5
	global_load_dwordx4 v[152:155], v[14:15], off
	global_load_dwordx4 v[156:159], v[16:17], off
	global_load_dwordx4 v[160:163], v[18:19], off
	global_load_dwordx4 v[164:167], v[20:21], off
	global_load_dwordx4 v[168:171], v[22:23], off
	global_load_dwordx4 v[172:175], v[24:25], off
	global_load_dwordx4 v[176:179], v[26:27], off
	s_waitcnt vmcnt(0)
